# attention flash loops: s_setprio 1 during the MFMA stage (PV + QK), 0 at its end
# speedup vs baseline: 1.0047x; 1.0047x over previous
; #define LAS __attribute__((address_space(3)))
; #define VM_WAIT() asm volatile("s_waitcnt vmcnt(0)" ::: "memory")
; #define SBAR() __builtin_amdgcn_sched_barrier(0)
; template <int OFF> __device__ __forceinline__ s16x4 tr_read(int vb) { s16x4 r; asm volatile("ds_read_b64_tr_b16 %0, %1 offset:%2" : "=&v"(r) : "v"(vb), "i"(OFF) : "memory"); return r; }
; __device__ __forceinline__ void qkt(f32x16& p0, f32x16& p1, const LAS char* Ks, const bf16x8 (&qr)[8], int r32, int hi) {
;     p0 = f32x16{}; p1 = f32x16{};
; #pragma unroll
;     for (int d0 = 0; d0 < 8; ++d0) { const int cb = (d0 * 16 + hi * 8) * 2;
;         const bf16x8 b0 = *(const LAS bf16x8*)(Ks + KSWZ(r32, cb));
;         const bf16x8 b1 = *(const LAS bf16x8*)(Ks + KSWZ(32 + r32, cb));
;         p0 = __builtin_amdgcn_mfma_f32_32x32x16_bf16(b0, qr[d0], p0, 0, 0, 0);
;         p1 = __builtin_amdgcn_mfma_f32_32x32x16_bf16(b1, qr[d0], p1, 0, 0, 0);
;         if (d0 == 3) SBAR(); }
; }
; template <int D0> __device__ __forceinline__ void pv_one(f32x16& od, int vb, bf16x8 pa0, bf16x8 pa1, bf16x8 pa2, bf16x8 pa3) {
;     const s16x4 l0 = tr_read<v_rd_off(D0, 0, 0)>(vb), h0 = tr_read<v_rd_off(D0, 0, 1)>(vb), l1 = tr_read<v_rd_off(D0, 1, 0)>(vb), h1 = tr_read<v_rd_off(D0, 1, 1)>(vb);
;     const s16x4 l2 = tr_read<v_rd_off(D0, 2, 0)>(vb), h2 = tr_read<v_rd_off(D0, 2, 1)>(vb), l3 = tr_read<v_rd_off(D0, 3, 0)>(vb), h3 = tr_read<v_rd_off(D0, 3, 1)>(vb);
;     asm volatile("s_waitcnt lgkmcnt(0)" ::: "memory"); SBAR();
;     ...
;     od = __builtin_amdgcn_mfma_f32_32x32x16_bf16(pa0, PK(l0, h0), od, 0, 0, 0);
;     od = __builtin_amdgcn_mfma_f32_32x32x16_bf16(pa1, PK(l1, h1), od, 0, 0, 0);
;     od = __builtin_amdgcn_mfma_f32_32x32x16_bf16(pa2, PK(l2, h2), od, 0, 0, 0);
;     od = __builtin_amdgcn_mfma_f32_32x32x16_bf16(pa3, PK(l3, h3), od, 0, 0, 0);
;     ...
; }
; template <int MODE> ...
;     ...
;     for (int i = 0; i < n; ++i) {
;         const int bcur = __builtin_amdgcn_readfirstlane(list[i]);
;         const int pslot = (buf == 0) ? 2 : buf - 1;
;         const int nslot = (buf == 2) ? 0 : buf + 1;
;         if (half == 0 && i + 1 >= 3 && i + 1 < n) DMA(i + 1, nslot);
;         if (i > 0) PV(pslot);
;         f32x16 p0, p1;
;         qkt(p0, p1, K_lds + buf * SHM, qr, r32, hi);
;         if (half == 1) VM_WAIT();
;         BAR();
;         if (half == 1 && i + 2 >= 3 && i + 2 < n) DMA(i + 2, pslot);
.LBB0_599:
	s_setprio 1
	s_lshl_b32 s29, s17, 14
	s_add_i32 s34, s29, 0xffffc000
	s_cmp_lg_u32 s17, 0
	s_cselect_b32 s17, s34, 0x8000
	v_add_u32_e32 v144, s17, v165
	ds_read_b64_tr_b16 v[84:85], v144 offset:0
	ds_read_b64_tr_b16 v[86:87], v144 offset:0x800
	ds_read_b64_tr_b16 v[88:89], v144 offset:0x1000
	ds_read_b64_tr_b16 v[90:91], v144 offset:0x1800
	ds_read_b64_tr_b16 v[92:93], v144 offset:0x2000
	ds_read_b64_tr_b16 v[94:95], v144 offset:0x2800
	ds_read_b64_tr_b16 v[96:97], v144 offset:0x3000
	ds_read_b64_tr_b16 v[98:99], v144 offset:0x3800
	s_waitcnt lgkmcnt(0)
	s_nop 0
	v_mfma_f32_32x32x16_bf16 v[20:35], v[72:75], v[84:87], v[20:35]
	ds_read_b64_tr_b16 v[84:85], v144 offset:0x200
	ds_read_b64_tr_b16 v[86:87], v144 offset:0xa00
	v_add_u32_e32 v246, s29, v148
	v_add_u32_e32 v247, v246, v149
	ds_read_b128 v[212:215], v247 offset:49152
	v_mfma_f32_32x32x16_bf16 v[20:35], v[76:79], v[88:91], v[20:35]
	ds_read_b64_tr_b16 v[88:89], v144 offset:0x1200
	ds_read_b64_tr_b16 v[90:91], v144 offset:0x1a00
	ds_read_b128 v[216:219], v247 offset:57344
	v_mfma_f32_32x32x16_bf16 v[20:35], v[80:83], v[92:95], v[20:35]
	ds_read_b64_tr_b16 v[92:93], v144 offset:0x2200
	ds_read_b64_tr_b16 v[94:95], v144 offset:0x2a00
	v_add_u32_e32 v247, v246, v150
	ds_read_b128 v[220:223], v247 offset:49152
	v_mfma_f32_32x32x16_bf16 v[20:35], v[68:71], v[96:99], v[20:35]
	ds_read_b64_tr_b16 v[96:97], v144 offset:0x3200
	ds_read_b64_tr_b16 v[98:99], v144 offset:0x3a00
	ds_read_b128 v[224:227], v247 offset:57344
	s_waitcnt lgkmcnt(0)
	v_mfma_f32_32x32x16_bf16 v[36:51], v[72:75], v[84:87], v[36:51]
	ds_read_b64_tr_b16 v[84:85], v144 offset:0x400
	ds_read_b64_tr_b16 v[86:87], v144 offset:0xc00
	v_add_u32_e32 v247, v246, v151
	ds_read_b128 v[228:231], v247 offset:49152
	v_mfma_f32_32x32x16_bf16 v[36:51], v[76:79], v[88:91], v[36:51]
	ds_read_b64_tr_b16 v[88:89], v144 offset:0x1400
	ds_read_b64_tr_b16 v[90:91], v144 offset:0x1c00
	ds_read_b128 v[232:235], v247 offset:57344
	v_mfma_f32_32x32x16_bf16 v[36:51], v[80:83], v[92:95], v[36:51]
	ds_read_b64_tr_b16 v[92:93], v144 offset:0x2400
	ds_read_b64_tr_b16 v[94:95], v144 offset:0x2c00
	v_add_u32_e32 v247, v246, v167
	ds_read_b128 v[236:239], v247 offset:49152
	v_mfma_f32_32x32x16_bf16 v[36:51], v[68:71], v[96:99], v[36:51]
	ds_read_b64_tr_b16 v[96:97], v144 offset:0x3400
	ds_read_b64_tr_b16 v[98:99], v144 offset:0x3c00
	ds_read_b128 v[240:243], v247 offset:57344
	s_waitcnt lgkmcnt(0)
	v_mfma_f32_32x32x16_bf16 v[52:67], v[72:75], v[84:87], v[52:67]
	ds_read_b64_tr_b16 v[84:85], v144 offset:0x600
	ds_read_b64_tr_b16 v[86:87], v144 offset:0xe00
	v_mfma_f32_32x32x16_bf16 v[52:67], v[76:79], v[88:91], v[52:67]
	ds_read_b64_tr_b16 v[88:89], v144 offset:0x1600
	ds_read_b64_tr_b16 v[90:91], v144 offset:0x1e00
	v_mfma_f32_32x32x16_bf16 v[52:67], v[80:83], v[92:95], v[52:67]
	ds_read_b64_tr_b16 v[92:93], v144 offset:0x2600
	ds_read_b64_tr_b16 v[94:95], v144 offset:0x2e00
	v_mfma_f32_32x32x16_bf16 v[52:67], v[68:71], v[96:99], v[52:67]
	ds_read_b64_tr_b16 v[96:97], v144 offset:0x3600
	ds_read_b64_tr_b16 v[98:99], v144 offset:0x3e00
	s_waitcnt lgkmcnt(0)
	v_mfma_f32_32x32x16_bf16 v[4:19], v[72:75], v[84:87], v[4:19]
	v_mfma_f32_32x32x16_bf16 v[4:19], v[76:79], v[88:91], v[4:19]
	v_mfma_f32_32x32x16_bf16 v[4:19], v[80:83], v[92:95], v[4:19]
	v_mfma_f32_32x32x16_bf16 v[4:19], v[68:71], v[96:99], v[4:19]
	s_and_b64 vcc, exec, s[12:13]
	v_mfma_f32_32x32x16_bf16 v[68:83], v[212:215], v[124:127], 0
	v_add_u32_e32 v247, v246, v169
	ds_read_b128 v[212:215], v247 offset:49152
	v_mfma_f32_32x32x16_bf16 v[84:99], v[216:219], v[124:127], 0
	ds_read_b128 v[216:219], v247 offset:57344
	v_mfma_f32_32x32x16_bf16 v[68:83], v[220:223], v[100:103], v[68:83]
	v_add_u32_e32 v247, v246, v176
	ds_read_b128 v[220:223], v247 offset:49152
	v_mfma_f32_32x32x16_bf16 v[84:99], v[224:227], v[100:103], v[84:99]
	ds_read_b128 v[224:227], v247 offset:57344
	v_mfma_f32_32x32x16_bf16 v[68:83], v[228:231], v[104:107], v[68:83]
	v_add_u32_e32 v247, v246, v177
	ds_read_b128 v[228:231], v247 offset:49152
	v_mfma_f32_32x32x16_bf16 v[84:99], v[232:235], v[104:107], v[84:99]
	ds_read_b128 v[232:235], v247 offset:57344
	v_mfma_f32_32x32x16_bf16 v[68:83], v[236:239], v[108:111], v[68:83]
	v_add_u32_e32 v247, v246, v178
	ds_read_b128 v[236:239], v247 offset:49152
	v_mfma_f32_32x32x16_bf16 v[84:99], v[240:243], v[108:111], v[84:99]
	ds_read_b128 v[240:243], v247 offset:57344
	s_waitcnt lgkmcnt(7)
	v_mfma_f32_32x32x16_bf16 v[68:83], v[212:215], v[112:115], v[68:83]
	s_waitcnt lgkmcnt(6)
	v_mfma_f32_32x32x16_bf16 v[84:99], v[216:219], v[112:115], v[84:99]
	s_waitcnt lgkmcnt(5)
	v_mfma_f32_32x32x16_bf16 v[68:83], v[220:223], v[116:119], v[68:83]
	s_waitcnt lgkmcnt(4)
	v_mfma_f32_32x32x16_bf16 v[84:99], v[224:227], v[116:119], v[84:99]
	s_waitcnt lgkmcnt(3)
	v_mfma_f32_32x32x16_bf16 v[68:83], v[228:231], v[120:123], v[68:83]
	s_waitcnt lgkmcnt(2)
	v_mfma_f32_32x32x16_bf16 v[84:99], v[232:235], v[120:123], v[84:99]
	s_waitcnt lgkmcnt(1)
	v_mfma_f32_32x32x16_bf16 v[68:83], v[236:239], v[128:131], v[68:83]
	s_waitcnt lgkmcnt(0)
	v_mfma_f32_32x32x16_bf16 v[84:99], v[240:243], v[128:131], v[84:99]
	s_cbranch_vccnz .LBB0_601
	s_waitcnt vmcnt(0)
.LBB0_601:
	s_setprio 0
	s_barrier
	s_and_b64 vcc, exec, s[12:13]
	s_cbranch_vccnz .LBB0_604
	s_add_i32 s29, s28, 2
	s_cmp_ge_i32 s29, s18
	s_cbranch_scc1 .LBB0_604
	v_mov_b32_e32 v144, s27
	ds_read_b32 v144, v144
	s_waitcnt lgkmcnt(0)
	v_readfirstlane_b32 s34, v144
	s_ashr_i32 s35, s34, 31
	s_lshl_b64 s[34:35], s[34:35], 14
	s_add_u32 s36, s14, s34
	s_addc_u32 s37, s15, s35
	s_add_i32 s17, s21, s17
	s_add_i32 m0, s17, 0xc000
	v_lshl_add_u64 v[144:145], v[136:137], 1, s[36:37]
	global_load_lds_dwordx4 v[144:145], off
	s_add_i32 m0, s17, 0xc400
	s_add_u32 s34, s19, s34
	v_lshl_add_u64 v[144:145], v[140:141], 1, s[36:37]
	s_addc_u32 s35, s20, s35
	global_load_lds_dwordx4 v[144:145], off
	v_lshl_add_u64 v[144:145], v[138:139], 1, s[34:35]
	s_mov_b32 m0, s17
	s_movk_i32 s37, 0x1af
	global_load_lds_dwordx4 v[144:145], off
	v_lshl_add_u64 v[144:145], v[142:143], 1, s[34:35]
	s_add_i32 m0, s17, 0x400
	s_movk_i32 s36, 0x7f
	global_load_lds_dwordx4 v[144:145], off

; #define LAS __attribute__((address_space(3)))
; #define VM_WAIT() asm volatile("s_waitcnt vmcnt(0)" ::: "memory")
; #define SBAR() __builtin_amdgcn_sched_barrier(0)
; template <int OFF> __device__ __forceinline__ s16x4 tr_read(int vb) { s16x4 r; asm volatile("ds_read_b64_tr_b16 %0, %1 offset:%2" : "=&v"(r) : "v"(vb), "i"(OFF) : "memory"); return r; }
; __device__ __forceinline__ void qkt(f32x16& p0, f32x16& p1, const LAS char* Ks, const bf16x8 (&qr)[8], int r32, int hi) {
;     p0 = f32x16{}; p1 = f32x16{};
; #pragma unroll
;     for (int d0 = 0; d0 < 8; ++d0) { const int cb = (d0 * 16 + hi * 8) * 2;
;         const bf16x8 b0 = *(const LAS bf16x8*)(Ks + KSWZ(r32, cb));
;         const bf16x8 b1 = *(const LAS bf16x8*)(Ks + KSWZ(32 + r32, cb));
;         p0 = __builtin_amdgcn_mfma_f32_32x32x16_bf16(b0, qr[d0], p0, 0, 0, 0);
;         p1 = __builtin_amdgcn_mfma_f32_32x32x16_bf16(b1, qr[d0], p1, 0, 0, 0);
;         if (d0 == 3) SBAR(); }
; }
; template <int D0> __device__ __forceinline__ void pv_one(f32x16& od, int vb, bf16x8 pa0, bf16x8 pa1, bf16x8 pa2, bf16x8 pa3) {
;     const s16x4 l0 = tr_read<v_rd_off(D0, 0, 0)>(vb), h0 = tr_read<v_rd_off(D0, 0, 1)>(vb), l1 = tr_read<v_rd_off(D0, 1, 0)>(vb), h1 = tr_read<v_rd_off(D0, 1, 1)>(vb);
;     const s16x4 l2 = tr_read<v_rd_off(D0, 2, 0)>(vb), h2 = tr_read<v_rd_off(D0, 2, 1)>(vb), l3 = tr_read<v_rd_off(D0, 3, 0)>(vb), h3 = tr_read<v_rd_off(D0, 3, 1)>(vb);
;     asm volatile("s_waitcnt lgkmcnt(0)" ::: "memory"); SBAR();
;     ...
;     od = __builtin_amdgcn_mfma_f32_32x32x16_bf16(pa0, PK(l0, h0), od, 0, 0, 0);
;     od = __builtin_amdgcn_mfma_f32_32x32x16_bf16(pa1, PK(l1, h1), od, 0, 0, 0);
;     od = __builtin_amdgcn_mfma_f32_32x32x16_bf16(pa2, PK(l2, h2), od, 0, 0, 0);
;     od = __builtin_amdgcn_mfma_f32_32x32x16_bf16(pa3, PK(l3, h3), od, 0, 0, 0);
;     ...
; }
; template <int MODE> ...
;     ...
;     for (int i = 0; i < n; ++i) {
;         const int bcur = __builtin_amdgcn_readfirstlane(list[i]);
;         const int pslot = (buf == 0) ? 2 : buf - 1;
;         const int nslot = (buf == 2) ? 0 : buf + 1;
;         if (half == 0 && i + 1 >= 3 && i + 1 < n) DMA(i + 1, nslot);
;         if (i > 0) PV(pslot);
;         f32x16 p0, p1;
;         qkt(p0, p1, K_lds + buf * SHM, qr, r32, hi);
;         if (half == 1) VM_WAIT();
;         BAR();
;         if (half == 1 && i + 2 >= 3 && i + 2 < n) DMA(i + 2, pslot);
.LBB0_775:
	s_setprio 1
	s_lshl_b32 s18, s13, 14
	s_add_i32 s19, s18, 0xffffc000
	s_cmp_lg_u32 s13, 0
	s_cselect_b32 s13, s19, 0x8000
	v_add_u32_e32 v188, s13, v165
	ds_read_b64_tr_b16 v[84:85], v188 offset:0
	ds_read_b64_tr_b16 v[86:87], v188 offset:0x800
	ds_read_b64_tr_b16 v[88:89], v188 offset:0x1000
	ds_read_b64_tr_b16 v[90:91], v188 offset:0x1800
	ds_read_b64_tr_b16 v[92:93], v188 offset:0x2000
	ds_read_b64_tr_b16 v[94:95], v188 offset:0x2800
	ds_read_b64_tr_b16 v[96:97], v188 offset:0x3000
	ds_read_b64_tr_b16 v[98:99], v188 offset:0x3800
	s_waitcnt lgkmcnt(0)
	s_nop 0
	v_mfma_f32_32x32x16_bf16 v[20:35], v[72:75], v[84:87], v[20:35]
	ds_read_b64_tr_b16 v[84:85], v188 offset:0x200
	ds_read_b64_tr_b16 v[86:87], v188 offset:0xa00
	v_add_u32_e32 v246, s18, v173
	v_add_u32_e32 v247, v246, v174
	ds_read_b128 v[212:215], v247 offset:49152
	v_mfma_f32_32x32x16_bf16 v[20:35], v[76:79], v[88:91], v[20:35]
	ds_read_b64_tr_b16 v[88:89], v188 offset:0x1200
	ds_read_b64_tr_b16 v[90:91], v188 offset:0x1a00
	ds_read_b128 v[216:219], v247 offset:57344
	v_mfma_f32_32x32x16_bf16 v[20:35], v[80:83], v[92:95], v[20:35]
	ds_read_b64_tr_b16 v[92:93], v188 offset:0x2200
	ds_read_b64_tr_b16 v[94:95], v188 offset:0x2a00
	v_add_u32_e32 v247, v246, v175
	ds_read_b128 v[220:223], v247 offset:49152
	v_mfma_f32_32x32x16_bf16 v[20:35], v[68:71], v[96:99], v[20:35]
	ds_read_b64_tr_b16 v[96:97], v188 offset:0x3200
	ds_read_b64_tr_b16 v[98:99], v188 offset:0x3a00
	ds_read_b128 v[224:227], v247 offset:57344
	s_waitcnt lgkmcnt(0)
	v_mfma_f32_32x32x16_bf16 v[36:51], v[72:75], v[84:87], v[36:51]
	ds_read_b64_tr_b16 v[84:85], v188 offset:0x400
	ds_read_b64_tr_b16 v[86:87], v188 offset:0xc00
	v_add_u32_e32 v247, v246, v176
	ds_read_b128 v[228:231], v247 offset:49152
	v_mfma_f32_32x32x16_bf16 v[36:51], v[76:79], v[88:91], v[36:51]
	ds_read_b64_tr_b16 v[88:89], v188 offset:0x1400
	ds_read_b64_tr_b16 v[90:91], v188 offset:0x1c00
	ds_read_b128 v[232:235], v247 offset:57344
	v_mfma_f32_32x32x16_bf16 v[36:51], v[80:83], v[92:95], v[36:51]
	ds_read_b64_tr_b16 v[92:93], v188 offset:0x2400
	ds_read_b64_tr_b16 v[94:95], v188 offset:0x2c00
	v_add_u32_e32 v247, v246, v177
	ds_read_b128 v[236:239], v247 offset:49152
	v_mfma_f32_32x32x16_bf16 v[36:51], v[68:71], v[96:99], v[36:51]
	ds_read_b64_tr_b16 v[96:97], v188 offset:0x3400
	ds_read_b64_tr_b16 v[98:99], v188 offset:0x3c00
	ds_read_b128 v[240:243], v247 offset:57344
	s_waitcnt lgkmcnt(0)
	v_mfma_f32_32x32x16_bf16 v[52:67], v[72:75], v[84:87], v[52:67]
	ds_read_b64_tr_b16 v[84:85], v188 offset:0x600
	ds_read_b64_tr_b16 v[86:87], v188 offset:0xe00
	v_mfma_f32_32x32x16_bf16 v[52:67], v[76:79], v[88:91], v[52:67]
	ds_read_b64_tr_b16 v[88:89], v188 offset:0x1600
	ds_read_b64_tr_b16 v[90:91], v188 offset:0x1e00
	v_mfma_f32_32x32x16_bf16 v[52:67], v[80:83], v[92:95], v[52:67]
	ds_read_b64_tr_b16 v[92:93], v188 offset:0x2600
	ds_read_b64_tr_b16 v[94:95], v188 offset:0x2e00
	v_mfma_f32_32x32x16_bf16 v[52:67], v[68:71], v[96:99], v[52:67]
	ds_read_b64_tr_b16 v[96:97], v188 offset:0x3600
	ds_read_b64_tr_b16 v[98:99], v188 offset:0x3e00
	s_waitcnt lgkmcnt(0)
	v_mfma_f32_32x32x16_bf16 v[4:19], v[72:75], v[84:87], v[4:19]
	v_mfma_f32_32x32x16_bf16 v[4:19], v[76:79], v[88:91], v[4:19]
	v_mfma_f32_32x32x16_bf16 v[4:19], v[80:83], v[92:95], v[4:19]
	v_mfma_f32_32x32x16_bf16 v[4:19], v[68:71], v[96:99], v[4:19]
	s_and_b64 vcc, exec, s[10:11]
	v_mfma_f32_32x32x16_bf16 v[68:83], v[212:215], v[124:127], 0
	v_add_u32_e32 v247, v246, v178
	ds_read_b128 v[212:215], v247 offset:49152
	v_mfma_f32_32x32x16_bf16 v[84:99], v[216:219], v[124:127], 0
	ds_read_b128 v[216:219], v247 offset:57344
	v_mfma_f32_32x32x16_bf16 v[68:83], v[220:223], v[100:103], v[68:83]
	v_add_u32_e32 v247, v246, v179
	ds_read_b128 v[220:223], v247 offset:49152
	v_mfma_f32_32x32x16_bf16 v[84:99], v[224:227], v[100:103], v[84:99]
	ds_read_b128 v[224:227], v247 offset:57344
	v_mfma_f32_32x32x16_bf16 v[68:83], v[228:231], v[104:107], v[68:83]
	v_add_u32_e32 v247, v246, v180
	ds_read_b128 v[228:231], v247 offset:49152
	v_mfma_f32_32x32x16_bf16 v[84:99], v[232:235], v[104:107], v[84:99]
	ds_read_b128 v[232:235], v247 offset:57344
	v_mfma_f32_32x32x16_bf16 v[68:83], v[236:239], v[108:111], v[68:83]
	v_add_u32_e32 v247, v246, v181
	ds_read_b128 v[236:239], v247 offset:49152
	v_mfma_f32_32x32x16_bf16 v[84:99], v[240:243], v[108:111], v[84:99]
	ds_read_b128 v[240:243], v247 offset:57344
	s_waitcnt lgkmcnt(7)
	v_mfma_f32_32x32x16_bf16 v[68:83], v[212:215], v[112:115], v[68:83]
	s_waitcnt lgkmcnt(6)
	v_mfma_f32_32x32x16_bf16 v[84:99], v[216:219], v[112:115], v[84:99]
	s_waitcnt lgkmcnt(5)
	v_mfma_f32_32x32x16_bf16 v[68:83], v[220:223], v[116:119], v[68:83]
	s_waitcnt lgkmcnt(4)
	v_mfma_f32_32x32x16_bf16 v[84:99], v[224:227], v[116:119], v[84:99]
	s_waitcnt lgkmcnt(3)
	v_mfma_f32_32x32x16_bf16 v[68:83], v[228:231], v[120:123], v[68:83]
	s_waitcnt lgkmcnt(2)
	v_mfma_f32_32x32x16_bf16 v[84:99], v[232:235], v[120:123], v[84:99]
	s_waitcnt lgkmcnt(1)
	v_mfma_f32_32x32x16_bf16 v[68:83], v[236:239], v[128:131], v[68:83]
	s_waitcnt lgkmcnt(0)
	v_mfma_f32_32x32x16_bf16 v[84:99], v[240:243], v[128:131], v[84:99]
	s_cbranch_vccnz .LBB0_777
	s_waitcnt vmcnt(0)
.LBB0_777:
	s_setprio 0
	s_barrier
	s_and_b64 vcc, exec, s[10:11]
	s_cbranch_vccnz .LBB0_780
	s_add_i32 s18, s17, 2
	s_cmp_ge_i32 s18, s6
	s_cbranch_scc1 .LBB0_780
	v_mov_b32_e32 v188, s7
	ds_read_b32 v188, v188
	s_mov_b64 s[20:21], 0x800
	s_waitcnt lgkmcnt(0)
	v_readfirstlane_b32 s18, v188
	s_mul_hi_i32 s19, s18, 0x1e8000
	s_mul_i32 s18, s18, 0x1e8000
	s_add_u32 s18, s14, s18
	s_addc_u32 s19, s15, s19
	s_add_i32 s13, s90, s13
	v_lshl_add_u64 v[188:189], v[152:153], 1, s[18:19]
	s_add_i32 m0, s13, 0xc000
	v_lshl_add_u64 v[188:189], v[188:189], 0, s[20:21]
	global_load_lds_dwordx4 v[188:189], off
	v_lshl_add_u64 v[188:189], v[156:157], 1, s[18:19]
	v_lshl_add_u64 v[188:189], v[188:189], 0, s[20:21]
	s_add_i32 m0, s13, 0xc400
	s_mov_b64 s[20:21], 0xc00
	global_load_lds_dwordx4 v[188:189], off
	v_lshl_add_u64 v[188:189], v[154:155], 1, s[18:19]
	v_lshl_add_u64 v[188:189], v[188:189], 0, s[20:21]
	s_mov_b32 m0, s13
	s_nop 0
	global_load_lds_dwordx4 v[188:189], off
	v_lshl_add_u64 v[188:189], v[158:159], 1, s[18:19]
	v_lshl_add_u64 v[188:189], v[188:189], 0, s[20:21]
	s_add_i32 m0, s13, 0x400
	s_nop 0
	global_load_lds_dwordx4 v[188:189], off

; #define LAS __attribute__((address_space(3)))
; #define VM_WAIT() asm volatile("s_waitcnt vmcnt(0)" ::: "memory")
; #define SBAR() __builtin_amdgcn_sched_barrier(0)
; template <int OFF> __device__ __forceinline__ s16x4 tr_read(int vb) { s16x4 r; asm volatile("ds_read_b64_tr_b16 %0, %1 offset:%2" : "=&v"(r) : "v"(vb), "i"(OFF) : "memory"); return r; }
; __device__ __forceinline__ void qkt(f32x16& p0, f32x16& p1, const LAS char* Ks, const bf16x8 (&qr)[8], int r32, int hi) {
;     p0 = f32x16{}; p1 = f32x16{};
; #pragma unroll
;     for (int d0 = 0; d0 < 8; ++d0) { const int cb = (d0 * 16 + hi * 8) * 2;
;         const bf16x8 b0 = *(const LAS bf16x8*)(Ks + KSWZ(r32, cb));
;         const bf16x8 b1 = *(const LAS bf16x8*)(Ks + KSWZ(32 + r32, cb));
;         p0 = __builtin_amdgcn_mfma_f32_32x32x16_bf16(b0, qr[d0], p0, 0, 0, 0);
;         p1 = __builtin_amdgcn_mfma_f32_32x32x16_bf16(b1, qr[d0], p1, 0, 0, 0);
;         if (d0 == 3) SBAR(); }
; }
; template <int D0> __device__ __forceinline__ void pv_one(f32x16& od, int vb, bf16x8 pa0, bf16x8 pa1, bf16x8 pa2, bf16x8 pa3) {
;     const s16x4 l0 = tr_read<v_rd_off(D0, 0, 0)>(vb), h0 = tr_read<v_rd_off(D0, 0, 1)>(vb), l1 = tr_read<v_rd_off(D0, 1, 0)>(vb), h1 = tr_read<v_rd_off(D0, 1, 1)>(vb);
;     const s16x4 l2 = tr_read<v_rd_off(D0, 2, 0)>(vb), h2 = tr_read<v_rd_off(D0, 2, 1)>(vb), l3 = tr_read<v_rd_off(D0, 3, 0)>(vb), h3 = tr_read<v_rd_off(D0, 3, 1)>(vb);
;     asm volatile("s_waitcnt lgkmcnt(0)" ::: "memory"); SBAR();
;     ...
;     od = __builtin_amdgcn_mfma_f32_32x32x16_bf16(pa0, PK(l0, h0), od, 0, 0, 0);
;     od = __builtin_amdgcn_mfma_f32_32x32x16_bf16(pa1, PK(l1, h1), od, 0, 0, 0);
;     od = __builtin_amdgcn_mfma_f32_32x32x16_bf16(pa2, PK(l2, h2), od, 0, 0, 0);
;     od = __builtin_amdgcn_mfma_f32_32x32x16_bf16(pa3, PK(l3, h3), od, 0, 0, 0);
;     ...
; }
; template <int MODE> ...
;     ...
;     for (int i = 0; i < n; ++i) {
;         const int bcur = __builtin_amdgcn_readfirstlane(list[i]);
;         const int pslot = (buf == 0) ? 2 : buf - 1;
;         const int nslot = (buf == 2) ? 0 : buf + 1;
;         if (half == 0 && i + 1 >= 3 && i + 1 < n) DMA(i + 1, nslot);
;         if (i > 0) PV(pslot);
;         f32x16 p0, p1;
;         qkt(p0, p1, K_lds + buf * SHM, qr, r32, hi);
;         if (half == 1) VM_WAIT();
;         BAR();
;         if (half == 1 && i + 2 >= 3 && i + 2 < n) DMA(i + 2, pslot);
.LBB0_833:
	s_setprio 1
	v_sub_co_u32_e64 v2, s[14:15], s13, 1
	s_and_b64 s[14:15], s[14:15], exec
	v_readfirstlane_b32 s14, v2
	s_cselect_b32 s14, 2, s14
	s_lshl_b32 s14, s14, 14
	v_add_u32_e32 v2, s14, v165
	ds_read_b64_tr_b16 v[84:85], v2 offset:0
	ds_read_b64_tr_b16 v[86:87], v2 offset:0x800
	ds_read_b64_tr_b16 v[88:89], v2 offset:0x1000
	ds_read_b64_tr_b16 v[90:91], v2 offset:0x1800
	ds_read_b64_tr_b16 v[92:93], v2 offset:0x2000
	ds_read_b64_tr_b16 v[94:95], v2 offset:0x2800
	ds_read_b64_tr_b16 v[96:97], v2 offset:0x3000
	ds_read_b64_tr_b16 v[98:99], v2 offset:0x3800
	s_waitcnt lgkmcnt(0)
	s_nop 0
	v_mfma_f32_32x32x16_bf16 v[20:35], v[72:75], v[84:87], v[20:35]
	ds_read_b64_tr_b16 v[84:85], v2 offset:0x200
	ds_read_b64_tr_b16 v[86:87], v2 offset:0xa00
	v_lshl_add_u32 v246, s13, 14, v170
	v_add_u32_e32 v247, v246, v171
	ds_read_b128 v[212:215], v247 offset:49152
	v_mfma_f32_32x32x16_bf16 v[20:35], v[76:79], v[88:91], v[20:35]
	ds_read_b64_tr_b16 v[88:89], v2 offset:0x1200
	ds_read_b64_tr_b16 v[90:91], v2 offset:0x1a00
	ds_read_b128 v[216:219], v247 offset:57344
	v_mfma_f32_32x32x16_bf16 v[20:35], v[80:83], v[92:95], v[20:35]
	ds_read_b64_tr_b16 v[92:93], v2 offset:0x2200
	ds_read_b64_tr_b16 v[94:95], v2 offset:0x2a00
	v_add_u32_e32 v247, v246, v172
	ds_read_b128 v[220:223], v247 offset:49152
	v_mfma_f32_32x32x16_bf16 v[20:35], v[68:71], v[96:99], v[20:35]
	ds_read_b64_tr_b16 v[96:97], v2 offset:0x3200
	ds_read_b64_tr_b16 v[98:99], v2 offset:0x3a00
	ds_read_b128 v[224:227], v247 offset:57344
	s_waitcnt lgkmcnt(0)
	v_mfma_f32_32x32x16_bf16 v[36:51], v[72:75], v[84:87], v[36:51]
	ds_read_b64_tr_b16 v[84:85], v2 offset:0x400
	ds_read_b64_tr_b16 v[86:87], v2 offset:0xc00
	v_add_u32_e32 v247, v246, v173
	ds_read_b128 v[228:231], v247 offset:49152
	v_mfma_f32_32x32x16_bf16 v[36:51], v[76:79], v[88:91], v[36:51]
	ds_read_b64_tr_b16 v[88:89], v2 offset:0x1400
	ds_read_b64_tr_b16 v[90:91], v2 offset:0x1c00
	ds_read_b128 v[232:235], v247 offset:57344
	v_mfma_f32_32x32x16_bf16 v[36:51], v[80:83], v[92:95], v[36:51]
	ds_read_b64_tr_b16 v[92:93], v2 offset:0x2400
	ds_read_b64_tr_b16 v[94:95], v2 offset:0x2c00
	v_add_u32_e32 v247, v246, v174
	ds_read_b128 v[236:239], v247 offset:49152
	v_mfma_f32_32x32x16_bf16 v[36:51], v[68:71], v[96:99], v[36:51]
	ds_read_b64_tr_b16 v[96:97], v2 offset:0x3400
	ds_read_b64_tr_b16 v[98:99], v2 offset:0x3c00
	ds_read_b128 v[240:243], v247 offset:57344
	s_waitcnt lgkmcnt(0)
	v_mfma_f32_32x32x16_bf16 v[52:67], v[72:75], v[84:87], v[52:67]
	ds_read_b64_tr_b16 v[84:85], v2 offset:0x600
	ds_read_b64_tr_b16 v[86:87], v2 offset:0xe00
	v_mfma_f32_32x32x16_bf16 v[52:67], v[76:79], v[88:91], v[52:67]
	ds_read_b64_tr_b16 v[88:89], v2 offset:0x1600
	ds_read_b64_tr_b16 v[90:91], v2 offset:0x1e00
	v_mfma_f32_32x32x16_bf16 v[52:67], v[80:83], v[92:95], v[52:67]
	ds_read_b64_tr_b16 v[92:93], v2 offset:0x2600
	ds_read_b64_tr_b16 v[94:95], v2 offset:0x2e00
	v_mfma_f32_32x32x16_bf16 v[52:67], v[68:71], v[96:99], v[52:67]
	ds_read_b64_tr_b16 v[96:97], v2 offset:0x3600
	ds_read_b64_tr_b16 v[98:99], v2 offset:0x3e00
	s_waitcnt lgkmcnt(0)
	v_mfma_f32_32x32x16_bf16 v[4:19], v[72:75], v[84:87], v[4:19]
	v_mfma_f32_32x32x16_bf16 v[4:19], v[76:79], v[88:91], v[4:19]
	v_mfma_f32_32x32x16_bf16 v[4:19], v[80:83], v[92:95], v[4:19]
	v_mfma_f32_32x32x16_bf16 v[4:19], v[68:71], v[96:99], v[4:19]
	s_and_b64 vcc, exec, s[10:11]
	v_mfma_f32_32x32x16_bf16 v[68:83], v[212:215], v[124:127], 0
	v_add_u32_e32 v247, v246, v175
	ds_read_b128 v[212:215], v247 offset:49152
	v_mfma_f32_32x32x16_bf16 v[84:99], v[216:219], v[124:127], 0
	ds_read_b128 v[216:219], v247 offset:57344
	v_mfma_f32_32x32x16_bf16 v[68:83], v[220:223], v[100:103], v[68:83]
	v_add_u32_e32 v247, v246, v176
	ds_read_b128 v[220:223], v247 offset:49152
	v_mfma_f32_32x32x16_bf16 v[84:99], v[224:227], v[100:103], v[84:99]
	ds_read_b128 v[224:227], v247 offset:57344
	v_mfma_f32_32x32x16_bf16 v[68:83], v[228:231], v[104:107], v[68:83]
	v_add_u32_e32 v247, v246, v177
	ds_read_b128 v[228:231], v247 offset:49152
	v_mfma_f32_32x32x16_bf16 v[84:99], v[232:235], v[104:107], v[84:99]
	ds_read_b128 v[232:235], v247 offset:57344
	v_mfma_f32_32x32x16_bf16 v[68:83], v[236:239], v[108:111], v[68:83]
	v_add_u32_e32 v247, v246, v178
	ds_read_b128 v[236:239], v247 offset:49152
	v_mfma_f32_32x32x16_bf16 v[84:99], v[240:243], v[108:111], v[84:99]
	ds_read_b128 v[240:243], v247 offset:57344
	s_waitcnt lgkmcnt(7)
	v_mfma_f32_32x32x16_bf16 v[68:83], v[212:215], v[112:115], v[68:83]
	s_waitcnt lgkmcnt(6)
	v_mfma_f32_32x32x16_bf16 v[84:99], v[216:219], v[112:115], v[84:99]
	s_waitcnt lgkmcnt(5)
	v_mfma_f32_32x32x16_bf16 v[68:83], v[220:223], v[116:119], v[68:83]
	s_waitcnt lgkmcnt(4)
	v_mfma_f32_32x32x16_bf16 v[84:99], v[224:227], v[116:119], v[84:99]
	s_waitcnt lgkmcnt(3)
	v_mfma_f32_32x32x16_bf16 v[68:83], v[228:231], v[120:123], v[68:83]
	s_waitcnt lgkmcnt(2)
	v_mfma_f32_32x32x16_bf16 v[84:99], v[232:235], v[120:123], v[84:99]
	s_waitcnt lgkmcnt(1)
	v_mfma_f32_32x32x16_bf16 v[68:83], v[236:239], v[128:131], v[68:83]
	s_waitcnt lgkmcnt(0)
	v_mfma_f32_32x32x16_bf16 v[84:99], v[240:243], v[128:131], v[84:99]
	s_cbranch_vccnz .LBB0_835
	s_waitcnt vmcnt(0)
.LBB0_835:
	s_setprio 0
	s_barrier
	s_and_b64 vcc, exec, s[10:11]
	s_cbranch_vccnz .LBB0_838
	s_add_i32 s13, s72, 2
	s_cmp_ge_i32 s13, s31
	s_cbranch_scc1 .LBB0_838
	v_mov_b32_e32 v2, s97
	ds_read_b32 v2, v2
	s_waitcnt lgkmcnt(0)
	v_readfirstlane_b32 s13, v2
	s_mul_hi_i32 s15, s13, 0x1e8000
	s_mul_i32 s13, s13, 0x1e8000
	s_add_u32 s16, s94, s13
	s_addc_u32 s17, s2, s15
	s_add_i32 s18, s90, s14
	s_add_i32 m0, s18, 0xc000
	v_lshl_add_u64 v[186:187], v[152:153], 1, s[16:17]
	global_load_lds_dwordx4 v[186:187], off
	s_add_i32 m0, s18, 0xc400
	s_add_u32 s14, s3, s13
	v_lshl_add_u64 v[186:187], v[156:157], 1, s[16:17]
	s_addc_u32 s15, s6, s15
	global_load_lds_dwordx4 v[186:187], off
	v_lshl_add_u64 v[186:187], v[154:155], 1, s[14:15]
	s_mov_b32 m0, s18
	s_nop 0
	global_load_lds_dwordx4 v[186:187], off
	v_lshl_add_u64 v[186:187], v[158:159], 1, s[14:15]
	s_add_i32 m0, s18, 0x400
	s_nop 0
	global_load_lds_dwordx4 v[186:187], off
